# fp8 expert GEMMs: block-scaled MFMA with unit scales replaced by the non-scaled v_mfma_f32_16x16x128_f8f6f4 (same fp8 e4m3 operands, f32 accumulate, identical results)
# baseline (speedup 1.0000x reference)
; #define LAS __attribute__((address_space(3)))
;     __device__ __forceinline__ void a_offs_idx(const Unit& u, const unsigned (&nat)[2], unsigned (&v)[4], const LAS int*) const { a_offs(u, nat, v); }
; #define PG8_STAGE_A(bufoff, gbase, h) do { _Pragma("unroll") for (int _i = 0; _i < 2; ++_i) PG8_GLDS(gbase, va[(h) * 2 + _i], ldsb + (bufoff) + ldsw + _i * 8192); } while (0)
; #define PG8_STAGE_B(bufoff, gbase) do { _Pragma("unroll") for (int _i = 0; _i < 2; ++_i) PG8_GLDS(gbase, voffB[_i], ldsb + (bufoff) + ldsw + _i * 8192); } while (0)
; #define PG8_LDA(dst, b, h) do { _Pragma("unroll") for (int m = 0; m < 4; ++m) _Pragma("unroll") for (int k = 0; k < 2; ++k) dst[m][k] = *(const LAS i32x4*)(lds + PG8_SA(b, h) + aoff + m * 2048 + k * 1024); } while (0)
; #define PG8_LDB(dst, b, h) do { _Pragma("unroll") for (int n = 0; n < 2; ++n) _Pragma("unroll") for (int k = 0; k < 2; ++k) dst[n][k] = *(const LAS i32x4*)(lds + PG8_SB(b, h) + boff + n * 2048 + k * 1024); } while (0)
; #define PG8_WAIT_V(n) asm volatile("s_waitcnt vmcnt(" #n ")" ::: "memory")
; #define PG8_WAIT_L(n) asm volatile("s_waitcnt lgkmcnt(" #n ")" ::: "memory")
; template <class Epi, class Sched>
; __device__ __forceinline__ void gemm_phase(LAS unsigned char* lds, const Sched& S, const Epi& E) {
;     ...
;             PG8_LDB(B0, 0, 0); PG8_LDB(B1, 0, 1); PG8_SCHED; PG8_LDA(At, 0, 0); PG8_STAGE_A(PG8_SA(1, 1), a1, 1);
;             PG8_WAIT_V(8); PG8_WAIT_L(0); PG8_BAR; PG8_MMA(0, 0, At, B0); PG8_MMA(0, 1, At, B1); PG8_BAR; PG8_SCHED;
;             if (last && has_next) S.a_offs_idx(nxt, natA, va, (const LAS int*)(lds + IDX_OFF));
;             PG8_LDA(At, 0, 1); PG8_STAGE_B(PG8_SB(0, 0), b2); PG8_STAGE_B(PG8_SB(0, 1), b2 + HSTEP); PG8_STAGE_A(PG8_SA(0, 0), a2, 0);
;             PG8_WAIT_V(8); PG8_WAIT_L(0); PG8_BAR; PG8_MMA(1, 0, At, B0); PG8_MMA(1, 1, At, B1); PG8_BAR; PG8_SCHED;
;             PG8_LDB(B0, 1, 0); PG8_LDB(B1, 1, 1); PG8_SCHED; PG8_LDA(At, 1, 0); PG8_STAGE_A(PG8_SA(0, 1), a2, 1);
;             PG8_WAIT_V(8); PG8_WAIT_L(0); PG8_BAR; PG8_MMA(0, 0, At, B0); PG8_MMA(0, 1, At, B1); PG8_BAR; PG8_SCHED;
;             PG8_LDA(At, 1, 1); PG8_STAGE_B(PG8_SB(1, 0), b3); PG8_STAGE_B(PG8_SB(1, 1), b3 + HSTEP); PG8_STAGE_A(PG8_SA(1, 0), a3, 0);
;             PG8_WAIT_V(8); PG8_WAIT_L(0); PG8_BAR; PG8_MMA(1, 0, At, B0); PG8_MMA(1, 1, At, B1); PG8_BAR; PG8_SCHED;
.LBB0_1010:
	s_add_u32 s58, s58, 0x100
	s_addc_u32 s59, s59, 0
	s_and_b64 s[62:63], s[60:61], exec
	s_cselect_b32 s66, s18, s58
	s_cselect_b32 s67, s19, s59
	s_add_u32 s62, s66, 0x80
	s_addc_u32 s63, s67, 0
	s_and_b64 s[60:61], s[60:61], exec
	s_cselect_b32 s60, s44, s41
	s_cselect_b32 s61, s45, s43
	s_add_u32 s64, s60, 0x80
	s_addc_u32 s65, s61, 0
	ds_read_b128 v[130:133], v214 offset:16384
	ds_read_b128 v[134:137], v214 offset:17408
	ds_read_b128 v[146:149], v214 offset:18432
	ds_read_b128 v[150:153], v214 offset:19456
	ds_read_b128 v[162:165], v214 offset:20480
	ds_read_b128 v[166:169], v214 offset:21504
	ds_read_b128 v[216:219], v214 offset:22528
	ds_read_b128 v[220:223], v214 offset:23552
	s_mov_b32 s12, m0
	s_mov_b32 m0, s30
	s_nop 0
	global_load_lds_dwordx4 v194, s[60:61]
	s_mov_b32 m0, s12
	s_nop 0
	s_mov_b32 s12, m0
	s_mov_b32 m0, s31
	s_nop 0
	global_load_lds_dwordx4 v201, s[60:61]
	s_mov_b32 m0, s12
	s_add_u32 s12, s60, 0x40000
	s_addc_u32 s13, s61, 0
	s_mov_b32 vcc_lo, m0
	s_mov_b32 m0, s36
	s_nop 0
	global_load_lds_dwordx4 v194, s[12:13]
	s_mov_b32 m0, vcc_lo
	s_nop 0
	s_mov_b32 vcc_lo, m0
	s_mov_b32 m0, s55
	s_nop 0
	global_load_lds_dwordx4 v201, s[12:13]
	s_mov_b32 m0, vcc_lo
	s_mov_b32 s12, m0
	s_mov_b32 m0, s29
	s_nop 0
	global_load_lds_dwordx4 v204, s[66:67]
	s_mov_b32 m0, s12
	s_nop 0
	s_mov_b32 s12, m0
	s_mov_b32 m0, s85
	s_nop 0
	global_load_lds_dwordx4 v205, s[66:67]
	s_mov_b32 m0, s12
	s_waitcnt vmcnt(8)
	s_waitcnt lgkmcnt(0)
	s_barrier
	s_setprio 1
	s_waitcnt lgkmcnt(6)
	v_mfma_f32_16x16x128_f8f6f4 v[126:129], v[18:25], v[130:137], v[126:129]
	v_mfma_f32_16x16x128_f8f6f4 v[122:125], v[26:33], v[130:137], v[122:125]
	s_waitcnt lgkmcnt(4)
	v_mfma_f32_16x16x128_f8f6f4 v[110:113], v[18:25], v[146:153], v[110:113]
	v_mfma_f32_16x16x128_f8f6f4 v[106:109], v[26:33], v[146:153], v[106:109]
	s_waitcnt lgkmcnt(2)
	v_mfma_f32_16x16x128_f8f6f4 v[224:227], v[18:25], v[162:169], v[94:97]
	v_mfma_f32_16x16x128_f8f6f4 v[228:231], v[26:33], v[162:169], v[90:93]
	s_waitcnt lgkmcnt(0)
	v_mfma_f32_16x16x128_f8f6f4 v[232:235], v[18:25], v[216:223], v[78:81]
	v_mfma_f32_16x16x128_f8f6f4 v[236:239], v[26:33], v[216:223], v[74:77]
	s_setprio 0
	s_setprio 1
	v_mfma_f32_16x16x128_f8f6f4 v[118:121], v[2:9], v[130:137], v[118:121]
	v_mfma_f32_16x16x128_f8f6f4 v[114:117], v[10:17], v[130:137], v[114:117]
	v_mfma_f32_16x16x128_f8f6f4 v[102:105], v[2:9], v[146:153], v[102:105]
	v_mfma_f32_16x16x128_f8f6f4 v[98:101], v[10:17], v[146:153], v[98:101]
	v_mfma_f32_16x16x128_f8f6f4 v[240:243], v[2:9], v[162:169], v[86:89]
	v_mfma_f32_16x16x128_f8f6f4 v[244:247], v[10:17], v[162:169], v[82:85]
	v_mfma_f32_16x16x128_f8f6f4 v[248:251], v[2:9], v[216:223], v[70:73]
	v_mfma_f32_16x16x128_f8f6f4 v[216:219], v[10:17], v[216:223], v[66:69]
	s_setprio 0
	s_barrier
	v_add_u32_e32 v14, 0x18000, v213
	v_add_u32_e32 v30, 0x1c000, v213
	ds_read_b128 v[2:5], v14
	ds_read_b128 v[6:9], v14 offset:1024
	ds_read_b128 v[10:13], v14 offset:2048
	ds_read_b128 v[14:17], v14 offset:3072
	ds_read_b128 v[18:21], v30
	ds_read_b128 v[22:25], v30 offset:1024
	ds_read_b128 v[26:29], v30 offset:2048
	ds_read_b128 v[30:33], v30 offset:3072
	ds_read_b128 v[66:69], v214 offset:32768
	ds_read_b128 v[70:73], v214 offset:33792
	ds_read_b128 v[74:77], v214 offset:34816
	ds_read_b128 v[78:81], v214 offset:35840
	ds_read_b128 v[82:85], v214 offset:36864
	ds_read_b128 v[86:89], v214 offset:37888
	ds_read_b128 v[90:93], v214 offset:38912
	ds_read_b128 v[94:97], v214 offset:39936
	s_mov_b32 s12, m0
	s_mov_b32 m0, s16
	s_nop 0
	global_load_lds_dwordx4 v206, s[66:67]
	s_mov_b32 m0, s12
	s_nop 0
	s_mov_b32 s12, m0
	s_mov_b32 m0, s17
	s_nop 0
	global_load_lds_dwordx4 v207, s[66:67]
	s_mov_b32 m0, s12
	s_waitcnt vmcnt(8)
	s_waitcnt lgkmcnt(0)
	s_barrier
	s_setprio 1
	s_waitcnt lgkmcnt(6)
	v_mfma_f32_16x16x128_f8f6f4 v[190:193], v[2:9], v[66:73], v[190:193]
	v_mfma_f32_16x16x128_f8f6f4 v[186:189], v[10:17], v[66:73], v[186:189]
	s_waitcnt lgkmcnt(4)
	v_mfma_f32_16x16x128_f8f6f4 v[174:177], v[2:9], v[74:81], v[174:177]
	v_mfma_f32_16x16x128_f8f6f4 v[170:173], v[10:17], v[74:81], v[170:173]
	s_waitcnt lgkmcnt(2)
	v_mfma_f32_16x16x128_f8f6f4 v[158:161], v[2:9], v[82:89], v[158:161]
	v_mfma_f32_16x16x128_f8f6f4 v[154:157], v[10:17], v[82:89], v[154:157]
	s_waitcnt lgkmcnt(0)
	v_mfma_f32_16x16x128_f8f6f4 v[142:145], v[2:9], v[90:97], v[142:145]
	v_mfma_f32_16x16x128_f8f6f4 v[138:141], v[10:17], v[90:97], v[138:141]
	s_setprio 0
	s_setprio 1
	v_mfma_f32_16x16x128_f8f6f4 v[182:185], v[18:25], v[66:73], v[182:185]
	v_mfma_f32_16x16x128_f8f6f4 v[178:181], v[26:33], v[66:73], v[58:61]
	v_mfma_f32_16x16x128_f8f6f4 v[166:169], v[18:25], v[74:81], v[62:65]
	v_mfma_f32_16x16x128_f8f6f4 v[162:165], v[26:33], v[74:81], v[50:53]
	v_mfma_f32_16x16x128_f8f6f4 v[150:153], v[18:25], v[82:89], v[54:57]
	v_mfma_f32_16x16x128_f8f6f4 v[146:149], v[26:33], v[82:89], v[42:45]
	v_mfma_f32_16x16x128_f8f6f4 v[134:137], v[18:25], v[90:97], v[46:49]
	v_mfma_f32_16x16x128_f8f6f4 v[130:133], v[26:33], v[90:97], v[34:37]
	s_setprio 0
	s_barrier
; #define LAS __attribute__((address_space(3)))
;     __device__ __forceinline__ void a_offs_idx(const Unit& u, const unsigned (&nat)[2], unsigned (&v)[4], const LAS int*) const { a_offs(u, nat, v); }
; #define PG8_STAGE_A(bufoff, gbase, h) do { _Pragma("unroll") for (int _i = 0; _i < 2; ++_i) PG8_GLDS(gbase, va[(h) * 2 + _i], ldsb + (bufoff) + ldsw + _i * 8192); } while (0)
; #define PG8_STAGE_B(bufoff, gbase) do { _Pragma("unroll") for (int _i = 0; _i < 2; ++_i) PG8_GLDS(gbase, voffB[_i], ldsb + (bufoff) + ldsw + _i * 8192); } while (0)
; #define PG8_LDA(dst, b, h) do { _Pragma("unroll") for (int m = 0; m < 4; ++m) _Pragma("unroll") for (int k = 0; k < 2; ++k) dst[m][k] = *(const LAS i32x4*)(lds + PG8_SA(b, h) + aoff + m * 2048 + k * 1024); } while (0)
; #define PG8_LDB(dst, b, h) do { _Pragma("unroll") for (int n = 0; n < 2; ++n) _Pragma("unroll") for (int k = 0; k < 2; ++k) dst[n][k] = *(const LAS i32x4*)(lds + PG8_SB(b, h) + boff + n * 2048 + k * 1024); } while (0)
; #define PG8_WAIT_V(n) asm volatile("s_waitcnt vmcnt(" #n ")" ::: "memory")
; #define PG8_WAIT_L(n) asm volatile("s_waitcnt lgkmcnt(" #n ")" ::: "memory")
; #define PG8_BAR __builtin_amdgcn_s_barrier()
; #define PG8_SCHED __builtin_amdgcn_sched_barrier(0)
;     __device__ __forceinline__ void a_offs_idx(const Unit& u, const unsigned (&nat)[2], unsigned (&v)[4], const LAS int* idx) const {
;         if (!GATHER) { a_offs(u, nat, v); return; }
; #pragma unroll
;         for (int h = 0; h < 2; ++h)
; #pragma unroll
;             for (int i = 0; i < 2; ++i) v[h * 2 + i] = (unsigned)idx[h * HALF + (int)(nat[i] / ROWB)] * ROWB + nat[i] % ROWB;
;     }
; template <class Epi, class Sched>
; __device__ __forceinline__ void gemm_phase(LAS unsigned char* lds, const Sched& S, const Epi& E) {
;     ...
;             PG8_WAIT_V(8); PG8_WAIT_L(0); PG8_BAR; PG8_MMA(1, 0, At, B0); PG8_MMA(1, 1, At, B1); PG8_BAR; PG8_SCHED;
;             PG8_LDB(B0, 1, 0); PG8_LDB(B1, 1, 1); PG8_SCHED; PG8_LDA(At, 1, 0); PG8_STAGE_A(PG8_SA(0, 1), a2, 1);
;             PG8_WAIT_V(8); PG8_WAIT_L(0); PG8_BAR; PG8_MMA(0, 0, At, B0); PG8_MMA(0, 1, At, B1); PG8_BAR; PG8_SCHED;
;             PG8_LDA(At, 1, 1); PG8_STAGE_B(PG8_SB(1, 0), b3); PG8_STAGE_B(PG8_SB(1, 1), b3 + HSTEP); PG8_STAGE_A(PG8_SA(1, 0), a3, 0);
;             PG8_WAIT_V(8); PG8_WAIT_L(0); PG8_BAR; PG8_MMA(1, 0, At, B0); PG8_MMA(1, 1, At, B1); PG8_BAR; PG8_SCHED;
	s_nop 4
	ds_read_b128 v[34:37], v214 offset:49152
	ds_read_b128 v[38:41], v214 offset:50176
	ds_read_b128 v[42:45], v214 offset:51200
	ds_read_b128 v[46:49], v214 offset:52224
	ds_read_b128 v[50:53], v214 offset:53248
	ds_read_b128 v[54:57], v214 offset:54272
	ds_read_b128 v[58:61], v214 offset:55296
	ds_read_b128 v[62:65], v214 offset:56320
	s_mov_b32 s12, m0
	s_mov_b32 m0, s14
	s_nop 0
	global_load_lds_dwordx4 v194, s[64:65]
	s_mov_b32 m0, s12
	s_nop 0
	s_mov_b32 s12, m0
	s_mov_b32 m0, s26
	s_nop 0
	global_load_lds_dwordx4 v201, s[64:65]
	s_mov_b32 m0, s12
	s_add_u32 s12, s60, 0x40080
	s_addc_u32 s13, s61, 0
	s_mov_b32 s60, m0
	s_mov_b32 m0, s95
	s_nop 0
	global_load_lds_dwordx4 v194, s[12:13]
	s_mov_b32 m0, s60
	s_nop 0
	s_mov_b32 s60, m0
	s_mov_b32 m0, s92
	s_nop 0
	global_load_lds_dwordx4 v201, s[12:13]
	s_mov_b32 m0, s60
	s_mov_b32 s12, m0
	s_mov_b32 m0, s27
	s_nop 0
	global_load_lds_dwordx4 v204, s[62:63]
	s_mov_b32 m0, s12
	s_nop 0
	s_mov_b32 s12, m0
	s_mov_b32 m0, s28
	s_nop 0
	global_load_lds_dwordx4 v205, s[62:63]
	s_mov_b32 m0, s12
	s_waitcnt vmcnt(8)
	s_waitcnt lgkmcnt(0)
	s_barrier
	s_setprio 1
	s_waitcnt lgkmcnt(6)
	v_mfma_f32_16x16x128_f8f6f4 v[126:129], v[2:9], v[34:41], v[126:129]
	v_mfma_f32_16x16x128_f8f6f4 v[122:125], v[10:17], v[34:41], v[122:125]
	s_waitcnt lgkmcnt(4)
	v_mfma_f32_16x16x128_f8f6f4 v[110:113], v[2:9], v[42:49], v[110:113]
	v_mfma_f32_16x16x128_f8f6f4 v[106:109], v[10:17], v[42:49], v[106:109]
	s_waitcnt lgkmcnt(2)
	v_mfma_f32_16x16x128_f8f6f4 v[94:97], v[2:9], v[50:57], v[224:227]
	v_mfma_f32_16x16x128_f8f6f4 v[90:93], v[10:17], v[50:57], v[228:231]
	s_waitcnt lgkmcnt(0)
	v_mfma_f32_16x16x128_f8f6f4 v[78:81], v[2:9], v[58:65], v[232:235]
	v_mfma_f32_16x16x128_f8f6f4 v[74:77], v[10:17], v[58:65], v[236:239]
	s_setprio 0
	s_setprio 1
	v_mfma_f32_16x16x128_f8f6f4 v[118:121], v[18:25], v[34:41], v[118:121]
	v_mfma_f32_16x16x128_f8f6f4 v[114:117], v[26:33], v[34:41], v[114:117]
	v_mfma_f32_16x16x128_f8f6f4 v[102:105], v[18:25], v[42:49], v[102:105]
	v_mfma_f32_16x16x128_f8f6f4 v[98:101], v[26:33], v[42:49], v[98:101]
	v_mfma_f32_16x16x128_f8f6f4 v[86:89], v[18:25], v[50:57], v[240:243]
	v_mfma_f32_16x16x128_f8f6f4 v[82:85], v[26:33], v[50:57], v[244:247]
	v_mfma_f32_16x16x128_f8f6f4 v[70:73], v[18:25], v[58:65], v[248:251]
	v_mfma_f32_16x16x128_f8f6f4 v[66:69], v[26:33], v[58:65], v[216:219]
	s_setprio 0
	s_barrier
	s_add_i32 s53, s53, 2
	s_add_u32 s41, s41, 0x100
	s_addc_u32 s43, s43, 0
	s_cmp_gt_u32 s53, 13
	s_cbranch_scc1 .LBB0_1013
.LBB0_1011:
	v_add_u32_e32 v2, 0x10000, v213
	v_add_u32_e32 v14, 0x14000, v213
	ds_read_b128 v[18:21], v2
	ds_read_b128 v[22:25], v2 offset:1024
	ds_read_b128 v[26:29], v2 offset:2048
	ds_read_b128 v[30:33], v2 offset:3072
	ds_read_b128 v[2:5], v14
	ds_read_b128 v[6:9], v14 offset:1024
	ds_read_b128 v[10:13], v14 offset:2048
	ds_read_b128 v[14:17], v14 offset:3072
	s_cmp_eq_u32 s53, 12
	s_cselect_b64 s[60:61], -1, 0
	s_add_u32 s62, s58, 0x80
	s_addc_u32 s63, s59, 0
	ds_read_b128 v[58:61], v214
	ds_read_b128 v[62:65], v214 offset:1024
	ds_read_b128 v[50:53], v214 offset:2048
	ds_read_b128 v[54:57], v214 offset:3072
	ds_read_b128 v[42:45], v214 offset:4096
	ds_read_b128 v[46:49], v214 offset:5120
	ds_read_b128 v[34:37], v214 offset:6144
	ds_read_b128 v[38:41], v214 offset:7168
	s_mov_b32 s12, m0
	s_mov_b32 m0, s96
	s_nop 0
	global_load_lds_dwordx4 v206, s[62:63]
	s_mov_b32 m0, s12
	s_nop 0
	s_mov_b32 s12, m0
	s_mov_b32 m0, s88
	s_nop 0
	global_load_lds_dwordx4 v207, s[62:63]
	s_mov_b32 m0, s12
	s_waitcnt vmcnt(8)
	s_waitcnt lgkmcnt(0)
	s_barrier
	s_setprio 1
	v_mfma_f32_16x16x128_f8f6f4 v[190:193], v[18:25], v[58:65], v[190:193]
	v_mfma_f32_16x16x128_f8f6f4 v[186:189], v[26:33], v[58:65], v[186:189]
	v_mfma_f32_16x16x128_f8f6f4 v[174:177], v[18:25], v[50:57], v[174:177]
	v_mfma_f32_16x16x128_f8f6f4 v[170:173], v[26:33], v[50:57], v[170:173]
	v_mfma_f32_16x16x128_f8f6f4 v[158:161], v[18:25], v[42:49], v[158:161]
	v_mfma_f32_16x16x128_f8f6f4 v[154:157], v[26:33], v[42:49], v[154:157]
	v_mfma_f32_16x16x128_f8f6f4 v[142:145], v[18:25], v[34:41], v[142:145]
	v_mfma_f32_16x16x128_f8f6f4 v[138:141], v[26:33], v[34:41], v[138:141]
	s_setprio 0
	s_setprio 1
	v_mfma_f32_16x16x128_f8f6f4 v[182:185], v[2:9], v[58:65], v[182:185]
	v_mfma_f32_16x16x128_f8f6f4 v[58:61], v[10:17], v[58:65], v[178:181]
	v_mfma_f32_16x16x128_f8f6f4 v[62:65], v[2:9], v[50:57], v[166:169]
	v_mfma_f32_16x16x128_f8f6f4 v[50:53], v[10:17], v[50:57], v[162:165]
	v_mfma_f32_16x16x128_f8f6f4 v[54:57], v[2:9], v[42:49], v[150:153]
	v_mfma_f32_16x16x128_f8f6f4 v[42:45], v[10:17], v[42:49], v[146:149]
	v_mfma_f32_16x16x128_f8f6f4 v[46:49], v[2:9], v[34:41], v[134:137]
	v_mfma_f32_16x16x128_f8f6f4 v[34:37], v[10:17], v[34:41], v[130:133]
	s_setprio 0
	s_barrier
	s_and_b64 s[62:63], s[56:57], s[60:61]
	s_andn2_b64 vcc, exec, s[62:63]
	s_cbranch_vccnz .LBB0_1010
	ds_read_b32 v204, v209
	ds_read_b32 v205, v210
	ds_read_b32 v206, v211
	ds_read_b32 v207, v212
	s_waitcnt lgkmcnt(3)
	v_lshl_or_b32 v204, v204, 11, v202
	s_waitcnt lgkmcnt(2)
	v_lshl_or_b32 v205, v205, 11, v203
	s_waitcnt lgkmcnt(1)
	v_lshl_or_b32 v206, v206, 11, v202
	s_waitcnt lgkmcnt(0)
	v_lshl_or_b32 v207, v207, 11, v203
	s_branch .LBB0_1010

; #define LAS __attribute__((address_space(3)))
;     __device__ __forceinline__ void a_offs_idx(const Unit& u, const unsigned (&nat)[2], unsigned (&v)[4], const LAS int*) const { a_offs(u, nat, v); }
; #define PG8_STAGE_A(bufoff, gbase, h) do { _Pragma("unroll") for (int _i = 0; _i < 2; ++_i) PG8_GLDS(gbase, va[(h) * 2 + _i], ldsb + (bufoff) + ldsw + _i * 8192); } while (0)
; #define PG8_STAGE_B(bufoff, gbase) do { _Pragma("unroll") for (int _i = 0; _i < 2; ++_i) PG8_GLDS(gbase, voffB[_i], ldsb + (bufoff) + ldsw + _i * 8192); } while (0)
; #define PG8_LDA(dst, b, h) do { _Pragma("unroll") for (int m = 0; m < 4; ++m) _Pragma("unroll") for (int k = 0; k < 2; ++k) dst[m][k] = *(const LAS i32x4*)(lds + PG8_SA(b, h) + aoff + m * 2048 + k * 1024); } while (0)
; #define PG8_LDB(dst, b, h) do { _Pragma("unroll") for (int n = 0; n < 2; ++n) _Pragma("unroll") for (int k = 0; k < 2; ++k) dst[n][k] = *(const LAS i32x4*)(lds + PG8_SB(b, h) + boff + n * 2048 + k * 1024); } while (0)
; #define PG8_WAIT_V(n) asm volatile("s_waitcnt vmcnt(" #n ")" ::: "memory")
; #define PG8_WAIT_L(n) asm volatile("s_waitcnt lgkmcnt(" #n ")" ::: "memory")
; template <class Epi, class Sched>
; __device__ __forceinline__ void gemm_phase(LAS unsigned char* lds, const Sched& S, const Epi& E) {
;     ...
;             PG8_LDB(B0, 0, 0); PG8_LDB(B1, 0, 1); PG8_SCHED; PG8_LDA(At, 0, 0); PG8_STAGE_A(PG8_SA(1, 1), a1, 1);
;             PG8_WAIT_V(8); PG8_WAIT_L(0); PG8_BAR; PG8_MMA(0, 0, At, B0); PG8_MMA(0, 1, At, B1); PG8_BAR; PG8_SCHED;
;             if (last && has_next) S.a_offs_idx(nxt, natA, va, (const LAS int*)(lds + IDX_OFF));
;             PG8_LDA(At, 0, 1); PG8_STAGE_B(PG8_SB(0, 0), b2); PG8_STAGE_B(PG8_SB(0, 1), b2 + HSTEP); PG8_STAGE_A(PG8_SA(0, 0), a2, 0);
;             PG8_WAIT_V(8); PG8_WAIT_L(0); PG8_BAR; PG8_MMA(1, 0, At, B0); PG8_MMA(1, 1, At, B1); PG8_BAR; PG8_SCHED;
;             PG8_LDB(B0, 1, 0); PG8_LDB(B1, 1, 1); PG8_SCHED; PG8_LDA(At, 1, 0); PG8_STAGE_A(PG8_SA(0, 1), a2, 1);
;             PG8_WAIT_V(8); PG8_WAIT_L(0); PG8_BAR; PG8_MMA(0, 0, At, B0); PG8_MMA(0, 1, At, B1); PG8_BAR; PG8_SCHED;
;             PG8_LDA(At, 1, 1); PG8_STAGE_B(PG8_SB(1, 0), b3); PG8_STAGE_B(PG8_SB(1, 1), b3 + HSTEP); PG8_STAGE_A(PG8_SA(1, 0), a3, 0);
;             PG8_WAIT_V(8); PG8_WAIT_L(0); PG8_BAR; PG8_MMA(1, 0, At, B0); PG8_MMA(1, 1, At, B1); PG8_BAR; PG8_SCHED;
.LBB0_1464:
	v_add_u32_e32 v122, 0x10000, v153
	s_add_u32 s48, s44, 0x100
	ds_read_b128 v[156:159], v122
	ds_read_b128 v[160:163], v122 offset:1024
	ds_read_b128 v[164:167], v122 offset:2048
	ds_read_b128 v[168:171], v122 offset:3072
	v_add_u32_e32 v122, 0x14000, v153
	s_addc_u32 s49, s45, 0
	ds_read_b128 v[172:175], v122
	ds_read_b128 v[176:179], v122 offset:1024
	ds_read_b128 v[180:183], v122 offset:2048
	ds_read_b128 v[184:187], v122 offset:3072
	s_cmp_eq_u32 s35, 12
	s_cselect_b32 s56, s36, s48
	s_cselect_b32 s57, s37, s49
	s_cselect_b32 s54, s38, s27
	s_cselect_b32 s55, s39, s29
	s_add_u32 s52, s56, 0x80
	s_addc_u32 s53, s57, 0
	s_add_u32 s44, s44, 0x80
	s_addc_u32 s45, s45, 0
	ds_read_b128 v[188:191], v154
	ds_read_b128 v[192:195], v154 offset:1024
	ds_read_b128 v[196:199], v154 offset:2048
	ds_read_b128 v[200:203], v154 offset:3072
	ds_read_b128 v[204:207], v154 offset:4096
	ds_read_b128 v[208:211], v154 offset:5120
	ds_read_b128 v[212:215], v154 offset:6144
	ds_read_b128 v[216:219], v154 offset:7168
	s_mov_b32 s41, m0
	s_mov_b32 m0, s67
	s_nop 0
	global_load_lds_dwordx4 v151, s[44:45]
	s_mov_b32 m0, s41
	s_nop 0
	s_mov_b32 s41, m0
	s_mov_b32 m0, s61
	s_nop 0
	global_load_lds_dwordx4 v152, s[44:45]
	s_mov_b32 m0, s41
	s_waitcnt vmcnt(8)
	s_waitcnt lgkmcnt(0)
	s_barrier
	s_setprio 1
	s_waitcnt lgkmcnt(6)
	v_mfma_f32_16x16x128_f8f6f4 v[126:129], v[164:171], v[188:195], v[126:129]
	s_waitcnt lgkmcnt(4)
	v_mfma_f32_16x16x128_f8f6f4 v[118:121], v[156:163], v[196:203], v[118:121]
	v_mfma_f32_16x16x128_f8f6f4 v[114:117], v[164:171], v[196:203], v[114:117]
	s_waitcnt lgkmcnt(2)
	v_mfma_f32_16x16x128_f8f6f4 v[110:113], v[156:163], v[204:211], v[110:113]
	v_mfma_f32_16x16x128_f8f6f4 v[106:109], v[164:171], v[204:211], v[106:109]
	s_waitcnt lgkmcnt(0)
	v_mfma_f32_16x16x128_f8f6f4 v[102:105], v[156:163], v[212:219], v[102:105]
	v_mfma_f32_16x16x128_f8f6f4 v[98:101], v[164:171], v[212:219], v[98:101]
	v_mfma_f32_16x16x128_f8f6f4 v[122:125], v[156:163], v[188:195], v[130:133]
	s_setprio 0
	s_setprio 1
	s_add_u32 s44, s54, 0x80
	s_addc_u32 s45, s55, 0
	v_mfma_f32_16x16x128_f8f6f4 v[134:137], v[172:179], v[188:195], v[62:65]
	v_mfma_f32_16x16x128_f8f6f4 v[142:145], v[180:187], v[188:195], v[58:61]
	v_mfma_f32_16x16x128_f8f6f4 v[188:191], v[172:179], v[196:203], v[54:57]
	v_mfma_f32_16x16x128_f8f6f4 v[192:195], v[180:187], v[196:203], v[50:53]
	v_mfma_f32_16x16x128_f8f6f4 v[196:199], v[172:179], v[204:211], v[46:49]
	v_mfma_f32_16x16x128_f8f6f4 v[200:203], v[180:187], v[204:211], v[42:45]
	v_mfma_f32_16x16x128_f8f6f4 v[204:207], v[172:179], v[212:219], v[38:41]
	v_mfma_f32_16x16x128_f8f6f4 v[208:211], v[180:187], v[212:219], v[34:37]
	s_setprio 0
	s_barrier
	s_nop 4
	ds_read_b128 v[34:37], v154 offset:16384
	ds_read_b128 v[38:41], v154 offset:17408
	ds_read_b128 v[42:45], v154 offset:18432
	ds_read_b128 v[46:49], v154 offset:19456
	ds_read_b128 v[50:53], v154 offset:20480
	ds_read_b128 v[54:57], v154 offset:21504
	ds_read_b128 v[58:61], v154 offset:22528
	ds_read_b128 v[62:65], v154 offset:23552
	s_mov_b32 s41, m0
	s_mov_b32 m0, s16
	s_nop 0
	global_load_lds_dwordx4 v148, s[54:55]
	s_mov_b32 m0, s41
	s_add_u32 s88, s54, 0x40000
	s_mov_b32 s41, m0
	s_mov_b32 m0, s30
	s_nop 0
	global_load_lds_dwordx4 v150, s[54:55]
	s_mov_b32 m0, s41
	s_addc_u32 s89, s55, 0
	s_mov_b32 s41, m0
	s_mov_b32 m0, s31
	s_nop 0
	global_load_lds_dwordx4 v148, s[88:89]
	s_mov_b32 m0, s41
	s_nop 0
	s_mov_b32 s41, m0
	s_mov_b32 m0, s43
	s_nop 0
	global_load_lds_dwordx4 v150, s[88:89]
	s_mov_b32 m0, s41
	s_nop 0
	s_mov_b32 s41, m0
	s_mov_b32 m0, s14
	s_nop 0
	global_load_lds_dwordx4 v138, s[56:57]
	s_mov_b32 m0, s41
	s_nop 0
	s_mov_b32 s41, m0
	s_mov_b32 m0, s85
	s_nop 0
	global_load_lds_dwordx4 v149, s[56:57]
	s_mov_b32 m0, s41
	s_waitcnt vmcnt(8)
	s_waitcnt lgkmcnt(0)
	s_barrier
	s_setprio 1
	s_waitcnt lgkmcnt(6)
	v_mfma_f32_16x16x128_f8f6f4 v[94:97], v[156:163], v[34:41], v[94:97]
	v_mfma_f32_16x16x128_f8f6f4 v[90:93], v[164:171], v[34:41], v[90:93]
	s_waitcnt lgkmcnt(4)
	v_mfma_f32_16x16x128_f8f6f4 v[86:89], v[156:163], v[42:49], v[86:89]
	v_mfma_f32_16x16x128_f8f6f4 v[82:85], v[164:171], v[42:49], v[82:85]
	s_waitcnt lgkmcnt(2)
	v_mfma_f32_16x16x128_f8f6f4 v[78:81], v[156:163], v[50:57], v[78:81]
	v_mfma_f32_16x16x128_f8f6f4 v[74:77], v[164:171], v[50:57], v[74:77]
	s_waitcnt lgkmcnt(0)
	v_mfma_f32_16x16x128_f8f6f4 v[212:215], v[156:163], v[58:65], v[70:73]
	v_mfma_f32_16x16x128_f8f6f4 v[216:219], v[164:171], v[58:65], v[66:69]
	s_setprio 0
	s_setprio 1
	v_mfma_f32_16x16x128_f8f6f4 v[220:223], v[172:179], v[34:41], v[30:33]
	v_mfma_f32_16x16x128_f8f6f4 v[224:227], v[180:187], v[34:41], v[26:29]
	v_mfma_f32_16x16x128_f8f6f4 v[228:231], v[172:179], v[42:49], v[22:25]
	v_mfma_f32_16x16x128_f8f6f4 v[232:235], v[180:187], v[42:49], v[18:21]
	v_mfma_f32_16x16x128_f8f6f4 v[236:239], v[172:179], v[50:57], v[14:17]
	v_mfma_f32_16x16x128_f8f6f4 v[240:243], v[180:187], v[50:57], v[10:13]
	v_mfma_f32_16x16x128_f8f6f4 v[244:247], v[172:179], v[58:65], v[6:9]
	v_mfma_f32_16x16x128_f8f6f4 v[248:251], v[180:187], v[58:65], v[2:5]
	s_setprio 0
	s_barrier
; #define PG8_STAGE_A(bufoff, gbase, h) do { _Pragma("unroll") for (int _i = 0; _i < 2; ++_i) PG8_GLDS(gbase, va[(h) * 2 + _i], ldsb + (bufoff) + ldsw + _i * 8192); } while (0)
; #define PG8_STAGE_B(bufoff, gbase) do { _Pragma("unroll") for (int _i = 0; _i < 2; ++_i) PG8_GLDS(gbase, voffB[_i], ldsb + (bufoff) + ldsw + _i * 8192); } while (0)
; #define PG8_LDA(dst, b, h) do { _Pragma("unroll") for (int m = 0; m < 4; ++m) _Pragma("unroll") for (int k = 0; k < 2; ++k) dst[m][k] = *(const LAS i32x4*)(lds + PG8_SA(b, h) + aoff + m * 2048 + k * 1024); } while (0)
; #define PG8_LDB(dst, b, h) do { _Pragma("unroll") for (int n = 0; n < 2; ++n) _Pragma("unroll") for (int k = 0; k < 2; ++k) dst[n][k] = *(const LAS i32x4*)(lds + PG8_SB(b, h) + boff + n * 2048 + k * 1024); } while (0)
; #define PG8_WAIT_V(n) asm volatile("s_waitcnt vmcnt(" #n ")" ::: "memory")
; #define PG8_WAIT_L(n) asm volatile("s_waitcnt lgkmcnt(" #n ")" ::: "memory")
; #define PG8_BAR __builtin_amdgcn_s_barrier()
; #define PG8_SCHED __builtin_amdgcn_sched_barrier(0)
; template <class Epi, class Sched>
; __device__ __forceinline__ void gemm_phase(LAS unsigned char* lds, const Sched& S, const Epi& E) {
;     ...
;             PG8_LDB(B0, 1, 0); PG8_LDB(B1, 1, 1); PG8_SCHED; PG8_LDA(At, 1, 0); PG8_STAGE_A(PG8_SA(0, 1), a2, 1);
;             PG8_WAIT_V(8); PG8_WAIT_L(0); PG8_BAR; PG8_MMA(0, 0, At, B0); PG8_MMA(0, 1, At, B1); PG8_BAR; PG8_SCHED;
;             PG8_LDA(At, 1, 1); PG8_STAGE_B(PG8_SB(1, 0), b3); PG8_STAGE_B(PG8_SB(1, 1), b3 + HSTEP); PG8_STAGE_A(PG8_SA(1, 0), a3, 0);
;             PG8_WAIT_V(8); PG8_WAIT_L(0); PG8_BAR; PG8_MMA(1, 0, At, B0); PG8_MMA(1, 1, At, B1); PG8_BAR; PG8_SCHED;
;         }
	s_nop 1
	v_add_u32_e32 v14, 0x18000, v153
	v_add_u32_e32 v18, 0x1c000, v153
	s_nop 0
	ds_read_b128 v[2:5], v14
	ds_read_b128 v[6:9], v14 offset:1024
	ds_read_b128 v[10:13], v14 offset:2048
	ds_read_b128 v[14:17], v14 offset:3072
	ds_read_b128 v[156:159], v18
	ds_read_b128 v[160:163], v18 offset:1024
	ds_read_b128 v[164:167], v18 offset:2048
	ds_read_b128 v[168:171], v18 offset:3072
	ds_read_b128 v[18:21], v154 offset:32768
	ds_read_b128 v[22:25], v154 offset:33792
	ds_read_b128 v[26:29], v154 offset:34816
	ds_read_b128 v[30:33], v154 offset:35840
	ds_read_b128 v[34:37], v154 offset:36864
	ds_read_b128 v[38:41], v154 offset:37888
	ds_read_b128 v[66:69], v154 offset:38912
	ds_read_b128 v[70:73], v154 offset:39936
	s_mov_b32 s41, m0
	s_mov_b32 m0, s77
	s_nop 0
	global_load_lds_dwordx4 v151, s[56:57]
	s_mov_b32 m0, s41
	s_nop 0
	s_mov_b32 s41, m0
	s_mov_b32 m0, s79
	s_nop 0
	global_load_lds_dwordx4 v152, s[56:57]
	s_mov_b32 m0, s41
	s_waitcnt vmcnt(8)
	s_waitcnt lgkmcnt(0)
	s_barrier
	s_setprio 1
	s_waitcnt lgkmcnt(6)
	v_mfma_f32_16x16x128_f8f6f4 v[130:133], v[2:9], v[18:25], v[122:125]
	v_mfma_f32_16x16x128_f8f6f4 v[126:129], v[10:17], v[18:25], v[126:129]
	s_waitcnt lgkmcnt(4)
	v_mfma_f32_16x16x128_f8f6f4 v[118:121], v[2:9], v[26:33], v[118:121]
	v_mfma_f32_16x16x128_f8f6f4 v[114:117], v[10:17], v[26:33], v[114:117]
	s_waitcnt lgkmcnt(2)
	v_mfma_f32_16x16x128_f8f6f4 v[110:113], v[2:9], v[34:41], v[110:113]
	v_mfma_f32_16x16x128_f8f6f4 v[106:109], v[10:17], v[34:41], v[106:109]
	s_waitcnt lgkmcnt(0)
	v_mfma_f32_16x16x128_f8f6f4 v[102:105], v[2:9], v[66:73], v[102:105]
	v_mfma_f32_16x16x128_f8f6f4 v[98:101], v[10:17], v[66:73], v[98:101]
	s_setprio 0
	s_setprio 1
	v_mfma_f32_16x16x128_f8f6f4 v[62:65], v[156:163], v[18:25], v[134:137]
	v_mfma_f32_16x16x128_f8f6f4 v[58:61], v[164:171], v[18:25], v[142:145]
	v_mfma_f32_16x16x128_f8f6f4 v[54:57], v[156:163], v[26:33], v[188:191]
	v_mfma_f32_16x16x128_f8f6f4 v[50:53], v[164:171], v[26:33], v[192:195]
	v_mfma_f32_16x16x128_f8f6f4 v[46:49], v[156:163], v[34:41], v[196:199]
	v_mfma_f32_16x16x128_f8f6f4 v[42:45], v[164:171], v[34:41], v[200:203]
	v_mfma_f32_16x16x128_f8f6f4 v[38:41], v[156:163], v[66:73], v[204:207]
	v_mfma_f32_16x16x128_f8f6f4 v[34:37], v[164:171], v[66:73], v[208:211]
	s_setprio 0
	s_barrier
	ds_read_b128 v[18:21], v154 offset:49152
	ds_read_b128 v[22:25], v154 offset:50176
	ds_read_b128 v[172:175], v154 offset:51200
	ds_read_b128 v[176:179], v154 offset:52224
	ds_read_b128 v[180:183], v154 offset:53248
	ds_read_b128 v[184:187], v154 offset:54272
	ds_read_b128 v[188:191], v154 offset:55296
	ds_read_b128 v[192:195], v154 offset:56320
	s_mov_b32 s41, m0
	s_mov_b32 m0, s9
	s_nop 0
	global_load_lds_dwordx4 v148, s[44:45]
	s_mov_b32 m0, s41
	s_nop 0
	s_mov_b32 s41, m0
	s_mov_b32 m0, s96
	s_nop 0
	global_load_lds_dwordx4 v150, s[44:45]
	s_mov_b32 m0, s41
	s_add_u32 s44, s54, 0x40080
	s_addc_u32 s45, s55, 0
	s_mov_b32 s41, m0
	s_mov_b32 m0, s4
	s_nop 0
	global_load_lds_dwordx4 v148, s[44:45]
	s_mov_b32 m0, s41
	s_nop 0
	s_mov_b32 s41, m0
	s_mov_b32 m0, s5
	s_nop 0
	global_load_lds_dwordx4 v150, s[44:45]
	s_mov_b32 m0, s41
	s_nop 0
	s_mov_b32 s41, m0
	s_mov_b32 m0, s21
	s_nop 0
	global_load_lds_dwordx4 v138, s[52:53]
	s_mov_b32 m0, s41
	s_nop 0
	s_mov_b32 s41, m0
	s_mov_b32 m0, s82
	s_nop 0
	global_load_lds_dwordx4 v149, s[52:53]
	s_mov_b32 m0, s41
	s_waitcnt vmcnt(8)
	s_waitcnt lgkmcnt(0)
	s_barrier
	s_setprio 1
	s_waitcnt lgkmcnt(6)
	v_mfma_f32_16x16x128_f8f6f4 v[94:97], v[2:9], v[18:25], v[94:97]
	v_mfma_f32_16x16x128_f8f6f4 v[90:93], v[10:17], v[18:25], v[90:93]
	s_waitcnt lgkmcnt(4)
	v_mfma_f32_16x16x128_f8f6f4 v[86:89], v[2:9], v[172:179], v[86:89]
	v_mfma_f32_16x16x128_f8f6f4 v[82:85], v[10:17], v[172:179], v[82:85]
	s_waitcnt lgkmcnt(2)
	v_mfma_f32_16x16x128_f8f6f4 v[78:81], v[2:9], v[180:187], v[78:81]
	v_mfma_f32_16x16x128_f8f6f4 v[74:77], v[10:17], v[180:187], v[74:77]
	s_waitcnt lgkmcnt(0)
	v_mfma_f32_16x16x128_f8f6f4 v[70:73], v[2:9], v[188:195], v[212:215]
	v_mfma_f32_16x16x128_f8f6f4 v[66:69], v[10:17], v[188:195], v[216:219]
	s_setprio 0
	s_setprio 1
	v_mfma_f32_16x16x128_f8f6f4 v[30:33], v[156:163], v[18:25], v[220:223]
	v_mfma_f32_16x16x128_f8f6f4 v[26:29], v[164:171], v[18:25], v[224:227]
	v_mfma_f32_16x16x128_f8f6f4 v[22:25], v[156:163], v[172:179], v[228:231]
	v_mfma_f32_16x16x128_f8f6f4 v[18:21], v[164:171], v[172:179], v[232:235]
	v_mfma_f32_16x16x128_f8f6f4 v[14:17], v[156:163], v[180:187], v[236:239]
	v_mfma_f32_16x16x128_f8f6f4 v[10:13], v[164:171], v[180:187], v[240:243]
	v_mfma_f32_16x16x128_f8f6f4 v[6:9], v[156:163], v[188:195], v[244:247]
	v_mfma_f32_16x16x128_f8f6f4 v[2:5], v[164:171], v[188:195], v[248:251]
	s_setprio 0
	s_barrier
	s_add_i32 s35, s35, 2
	s_add_u32 s27, s27, 0x100
	s_addc_u32 s29, s29, 0
	s_cmp_gt_u32 s35, 13
	s_mov_b64 s[44:45], s[48:49]
	s_cbranch_scc0 .LBB0_1464
	s_and_b64 vcc, exec, s[24:25]
	s_cbranch_vccz .LBB0_1467
	s_barrier
